# MLA loop: cross-half combine of the tile max moved into the rare rescale path (the all-lanes threshold test is unchanged by it)
# speedup vs baseline: 1.0108x; 1.0031x over previous
; #define SBAR() __builtin_amdgcn_sched_barrier(0)
; #define SLOAD(i, j) do { const int _row = KROW(j); skn[i] = *(const bf16x8*)(Knp + (size_t)(_row + sr) * ldk + c8 * 8); sv[i] = *(const bf16x8*)(Vp + (size_t)(_row + sr) * ldv + c8 * 8); \
;         if (krw) skr[i] = *(const bf16x8*)(Krp + (size_t)(_row + sr2) * 32 + c4 * 8); } while (0)
; #define SWRITEO(boff, i) do { *(LAS bf16x8*)(lds + (boff) + kn_st) = skn[i]; *(LAS bf16x8*)(lds + (boff) + v_stw) = sv[i]; if (krw) *(LAS bf16x8*)(lds + (boff) + kr_st) = skr[i]; } while (0)
; #define PVO(boff) do { pv_one<0>(o0, vb0 + (boff), pa0, pa1, pa2, pa3); pv_one<1>(o1, vb0 + (boff), pa0, pa1, pa2, pa3); } while (0)
; #define SWAIT() asm volatile("s_waitcnt vmcnt(2)" ::: "memory")
; #define RESC(a) do { if (__any((a) < 1.f)) { _Pragma("unroll") for (int r = 0; r < 16; ++r) { o0[r] *= (a); o1[r] *= (a); } } } while (0)
; __device__ __forceinline__ float psm_max(const f32x16& p0, const f32x16& p1) {
;     float pmax = p0[0];
; #pragma unroll
;     for (int r = 1; r < 16; ++r) pmax = fmaxf(pmax, p0[r]);
; #pragma unroll
;     for (int r = 0; r < 16; ++r) pmax = fmaxf(pmax, p1[r]);
;     { auto rr = __builtin_amdgcn_permlane32_swap(__float_as_uint(pmax), __float_as_uint(pmax), false, false);
;       pmax = fmaxf(__uint_as_float(rr[0]), __uint_as_float(rr[1])); }
;     return pmax;
; }
; template <int DQK, bool FIXM> ...
;     ...
;     for (int j = 1; j + 1 < NT; j += 2) {
;         if (!NOBAR_PROBE) __syncthreads();
;         SBAR(); qkt<DQK>(pB0, pB1, lds + bK, qr, r32, hi, negm);
;         finishSM(pA0, pA1, alA, l_reg, pa0, pa1, pa2, pa3); SBAR();
;         SLOAD(1, j + 2); SBAR();
;         if constexpr (FIXM) pv_psm<true>(o0, o1, vb0 + bV, pa0, pa1, pa2, pa3, pB0, pB1, m_reg, negm, alB); else { PVO(bV); partialSM<false>(pB0, pB1, m_reg, negm, alB); }
;         SWAIT(); SWRITEO(bW, 0);
;         if (!FIXM) RESC(alB); ROT();
;         if (!NOBAR_PROBE) __syncthreads();
;         SBAR(); qkt<DQK>(pA0, pA1, lds + bK, qr, r32, hi, negm);
;         finishSM(pB0, pB1, alB, l_reg, pa0, pa1, pa2, pa3); SBAR();
;         if (j + 3 < NT) SLOAD(0, j + 3); SBAR();
;         if constexpr (FIXM) pv_psm<true>(o0, o1, vb0 + bV, pa0, pa1, pa2, pa3, pA0, pA1, m_reg, negm, alA); else { PVO(bV); partialSM<false>(pA0, pA1, m_reg, negm, alA); }
;         SWAIT(); SWRITEO(bW, 1);
;         if (!FIXM) RESC(alA); ROT();
;     }
.LBB0_523:
	s_waitcnt lgkmcnt(0)
	s_barrier
	ds_read_b128 v[4:7], v209 offset:20480
	ds_read_b128 v[8:11], v209 offset:24576
	ds_read_b128 v[174:177], v210 offset:20480
	ds_read_b128 v[246:249], v210 offset:24576
	ds_read_b128 v[250:253], v211 offset:20480
	ds_read_b128 v[78:81], v211 offset:24576
	ds_read_b128 v[12:15], v212 offset:20480
	v_exp_f32_e32 v98, v98
	v_exp_f32_e32 v99, v99
	v_exp_f32_e32 v100, v100
	v_exp_f32_e32 v101, v101
	v_exp_f32_e32 v102, v102
	v_exp_f32_e32 v103, v103
	v_exp_f32_e32 v104, v104
	v_exp_f32_e32 v105, v105
	s_waitcnt lgkmcnt(6)
	v_mfma_f32_32x32x16_bf16 v[130:145], v[4:7], v[166:169], v[82:97]
	ds_read_b128 v[4:7], v212 offset:24576
	v_exp_f32_e32 v106, v106
	v_exp_f32_e32 v107, v107
	v_exp_f32_e32 v108, v108
	v_cvt_pk_bf16_f32 v74, v243, v245
	s_waitcnt lgkmcnt(6)
	v_mfma_f32_32x32x16_bf16 v[114:129], v[8:11], v[166:169], v[82:97]
	ds_read_b128 v[8:11], v219 offset:28672
	v_exp_f32_e32 v109, v109
	v_exp_f32_e32 v110, v110
	v_exp_f32_e32 v111, v111
	v_cvt_pk_bf16_f32 v75, v241, v244
	s_waitcnt lgkmcnt(6)
	v_mfma_f32_32x32x16_bf16 v[130:145], v[174:177], v[162:165], v[130:145]
	ds_read_b128 v[174:177], v219 offset:30720
	v_exp_f32_e32 v112, v112
	v_exp_f32_e32 v113, v113
	v_cvt_pk_bf16_f32 v76, v239, v242
	v_cvt_pk_bf16_f32 v77, v238, v240
	v_add_f32_e32 v229, 0, v243
	v_add_f32_e32 v229, v245, v229
	s_waitcnt lgkmcnt(6)
	v_mfma_f32_32x32x16_bf16 v[114:129], v[246:249], v[162:165], v[114:129]
	ds_read_b128 v[246:249], v220 offset:28672
	v_cvt_pk_bf16_f32 v66, v236, v237
	v_cvt_pk_bf16_f32 v67, v233, v235
	v_add_f32_e32 v229, v241, v229
	v_add_f32_e32 v229, v244, v229
	v_add_f32_e32 v229, v239, v229
	v_add_f32_e32 v229, v242, v229
	s_waitcnt lgkmcnt(6)
	v_mfma_f32_32x32x16_bf16 v[130:145], v[250:253], v[158:161], v[130:145]
	ds_read_b128 v[250:253], v220 offset:30720
	v_cvt_pk_bf16_f32 v68, v231, v234
	v_cvt_pk_bf16_f32 v69, v230, v232
	v_add_f32_e32 v229, v238, v229
	v_add_f32_e32 v229, v240, v229
	v_add_f32_e32 v229, v236, v229
	v_add_f32_e32 v229, v237, v229
	s_waitcnt lgkmcnt(6)
	v_mfma_f32_32x32x16_bf16 v[114:129], v[78:81], v[158:161], v[114:129]
	v_add_f32_e32 v229, v233, v229
	v_add_f32_e32 v229, v235, v229
	v_add_f32_e32 v229, v231, v229
	v_add_f32_e32 v229, v234, v229
	v_add_f32_e32 v229, v230, v229
	v_add_f32_e32 v229, v232, v229
	s_waitcnt lgkmcnt(5)
	v_mfma_f32_32x32x16_bf16 v[130:145], v[12:15], v[154:157], v[130:145]
	ds_read_b64_tr_b16 v[230:231], v213 offset:0
	ds_read_b64_tr_b16 v[232:233], v213 offset:1024
	ds_read_b64_tr_b16 v[234:235], v213 offset:2048
	ds_read_b64_tr_b16 v[236:237], v213 offset:3072
	v_add_f32_e32 v229, v98, v229
	v_add_f32_e32 v229, v99, v229
	v_add_f32_e32 v229, v100, v229
	s_waitcnt lgkmcnt(8)
	v_mfma_f32_32x32x16_bf16 v[114:129], v[4:7], v[154:157], v[114:129]
	ds_read_b64_tr_b16 v[238:239], v213 offset:4096
	ds_read_b64_tr_b16 v[240:241], v213 offset:5120
	ds_read_b64_tr_b16 v[242:243], v213 offset:6144
	ds_read_b64_tr_b16 v[244:245], v213 offset:7168
	v_add_f32_e32 v229, v101, v229
	v_add_f32_e32 v229, v102, v229
	v_add_f32_e32 v229, v103, v229
	s_waitcnt lgkmcnt(11)
	v_mfma_f32_32x32x16_bf16 v[130:145], v[8:11], v[150:153], v[130:145]
	v_add_f32_e32 v229, v104, v229
	v_add_f32_e32 v229, v105, v229
	v_add_f32_e32 v229, v106, v229
	v_add_f32_e32 v229, v107, v229
	v_add_f32_e32 v229, v108, v229
	v_add_f32_e32 v229, v109, v229
	s_waitcnt lgkmcnt(10)
	v_mfma_f32_32x32x16_bf16 v[114:129], v[174:177], v[150:153], v[114:129]
	v_add_f32_e32 v229, v110, v229
	v_add_f32_e32 v229, v111, v229
	v_add_f32_e32 v229, v112, v229
	v_add_f32_e32 v228, v113, v229
	v_mov_b32_e32 v229, v228
	s_add_i32 s36, s35, -1
	s_cmp_lt_u32 s36, s30
	s_cselect_b32 s0, 0, s30
	s_cselect_b32 s1, s29, s34
	s_lshl_b32 s0, s0, 6
	s_sub_i32 s37, s1, s0
	s_lshl_b32 s1, s36, 6
	s_add_i32 s37, s37, s1
	s_lshl_b32 s0, s37, 6
	s_add_u32 s48, s44, s0
	s_addc_u32 s49, s45, 0
	s_lshl_b32 s0, s37, 11
	s_add_u32 s46, s42, s0
	s_addc_u32 s47, s43, 0
	global_load_dwordx4 v[174:177], v226, s[48:49]
	s_waitcnt lgkmcnt(9)
	v_mfma_f32_32x32x16_bf16 v[130:145], v[246:249], v[146:149], v[130:145]
	v_cvt_pk_bf16_f32 v70, v98, v99
	v_cvt_pk_bf16_f32 v71, v100, v101
	v_cvt_pk_bf16_f32 v72, v102, v103
	v_cvt_pk_bf16_f32 v73, v104, v105
	v_permlane32_swap_b32_e32 v228, v229
	global_load_dwordx4 v[8:11], v225, s[46:47]
	global_load_dwordx4 v[4:7], v225, s[46:47] offset:128
	s_waitcnt lgkmcnt(8)
	v_mfma_f32_32x32x16_bf16 v[114:129], v[250:253], v[146:149], v[114:129]
	v_cvt_pk_bf16_f32 v12, v106, v107
	v_cvt_pk_bf16_f32 v13, v108, v109
	v_cvt_pk_bf16_f32 v14, v110, v111
	v_cvt_pk_bf16_f32 v15, v112, v113
	ds_read_b64_tr_b16 v[78:79], v213 offset:512
	ds_read_b64_tr_b16 v[80:81], v213 offset:1536
	ds_read_b64_tr_b16 v[98:99], v213 offset:2560
	ds_read_b64_tr_b16 v[100:101], v213 offset:3584
	ds_read_b64_tr_b16 v[102:103], v213 offset:4608
	ds_read_b64_tr_b16 v[104:105], v213 offset:5632
	ds_read_b64_tr_b16 v[110:111], v213 offset:6656
	ds_read_b64_tr_b16 v[112:113], v213 offset:7680
	v_max3_f32 v2, v130, v131, v132
	v_max3_f32 v2, v2, v133, v134
	v_max3_f32 v2, v2, v135, v136
	v_max3_f32 v2, v2, v137, v138
	v_max3_f32 v2, v2, v139, v140
	v_max3_f32 v2, v2, v141, v142
	v_max3_f32 v2, v2, v143, v144
	v_max3_f32 v2, v2, v145, v114
	v_max3_f32 v2, v2, v115, v116
	s_waitcnt lgkmcnt(8)
	v_mfma_f32_32x32x16_bf16 v[50:65], v[230:233], v[74:77], v[50:65]
	v_max3_f32 v2, v2, v117, v118
	v_max3_f32 v2, v2, v119, v120
	v_max3_f32 v2, v2, v121, v122
	v_mfma_f32_32x32x16_bf16 v[50:65], v[234:237], v[66:69], v[50:65]
	v_max3_f32 v2, v2, v123, v124
	v_max3_f32 v2, v2, v125, v126
	v_max3_f32 v2, v2, v127, v128
	v_mfma_f32_32x32x16_bf16 v[50:65], v[238:241], v[70:73], v[50:65]
	v_max_f32_e32 v2, v2, v129
	v_mfma_f32_32x32x16_bf16 v[50:65], v[242:245], v[12:15], v[50:65]
	v_cmp_ge_f32_e32 vcc, s28, v2
	s_cmp_eq_u64 vcc, exec
	s_cbranch_scc0 .LBB0_542_0
	v_mov_b32_e32 v2, 1.0

; __device__ __forceinline__ float psm_max(const f32x16& p0, const f32x16& p1) {
;     float pmax = p0[0];
; #pragma unroll
;     for (int r = 1; r < 16; ++r) pmax = fmaxf(pmax, p0[r]);
; #pragma unroll
;     for (int r = 0; r < 16; ++r) pmax = fmaxf(pmax, p1[r]);
;     { auto rr = __builtin_amdgcn_permlane32_swap(__float_as_uint(pmax), __float_as_uint(pmax), false, false);
;       pmax = fmaxf(__uint_as_float(rr[0]), __uint_as_float(rr[1])); }
;     return pmax;
; }
.Lmla_b_ld_done_0:
	s_waitcnt lgkmcnt(8)
	v_mfma_f32_32x32x16_bf16 v[98:113], v[70:73], v[146:149], v[98:113]
	v_cvt_pk_bf16_f32 v118, v122, v123
	v_cvt_pk_bf16_f32 v119, v124, v125
	v_cvt_pk_bf16_f32 v120, v126, v127
	v_cvt_pk_bf16_f32 v121, v128, v129
	v_add_f32_e32 v126, v129, v252
	v_mov_b32_e32 v127, v126
	ds_read_b64_tr_b16 v[66:67], v213 offset:20992
	ds_read_b64_tr_b16 v[68:69], v213 offset:22016
	ds_read_b64_tr_b16 v[70:71], v213 offset:23040
	ds_read_b64_tr_b16 v[72:73], v213 offset:24064
	ds_read_b64_tr_b16 v[74:75], v213 offset:25088
	ds_read_b64_tr_b16 v[76:77], v213 offset:26112
	ds_read_b64_tr_b16 v[78:79], v213 offset:27136
	ds_read_b64_tr_b16 v[80:81], v213 offset:28160
	v_permlane32_swap_b32_e32 v126, v127
	v_max3_f32 v250, v130, v131, v132
	v_max3_f32 v250, v250, v133, v134
	v_max3_f32 v250, v250, v135, v136
	v_max3_f32 v250, v250, v137, v138
	v_max3_f32 v250, v250, v139, v140
	v_max3_f32 v250, v250, v141, v142
	v_max3_f32 v250, v250, v143, v144
	v_max3_f32 v250, v250, v145, v98
	v_max3_f32 v250, v250, v99, v100
	s_waitcnt lgkmcnt(8)
	v_mfma_f32_32x32x16_bf16 v[50:65], v[234:237], v[12:15], v[50:65]
	v_max3_f32 v250, v250, v101, v102
	v_max3_f32 v250, v250, v103, v104
	v_max3_f32 v250, v250, v105, v106
	v_mfma_f32_32x32x16_bf16 v[50:65], v[238:241], v[230:233], v[50:65]
	v_max3_f32 v250, v250, v107, v108
	v_max3_f32 v250, v250, v109, v110
	v_max3_f32 v250, v250, v111, v112
	v_mfma_f32_32x32x16_bf16 v[50:65], v[242:245], v[114:117], v[50:65]
	v_max_f32_e32 v250, v250, v113
	v_mfma_f32_32x32x16_bf16 v[50:65], v[246:249], v[118:121], v[50:65]
	v_cmp_ge_f32_e32 vcc, s28, v250
	s_cmp_eq_u64 vcc, exec
	v_mov_b32_e32 v16, 1.0
	s_cbranch_scc0 .LBB0_543_0

; #define SBAR() __builtin_amdgcn_sched_barrier(0)
; #define SLOAD(i, j) do { const int _row = KROW(j); skn[i] = *(const bf16x8*)(Knp + (size_t)(_row + sr) * ldk + c8 * 8); sv[i] = *(const bf16x8*)(Vp + (size_t)(_row + sr) * ldv + c8 * 8); \
;         if (krw) skr[i] = *(const bf16x8*)(Krp + (size_t)(_row + sr2) * 32 + c4 * 8); } while (0)
; #define SWRITEO(boff, i) do { *(LAS bf16x8*)(lds + (boff) + kn_st) = skn[i]; *(LAS bf16x8*)(lds + (boff) + v_stw) = sv[i]; if (krw) *(LAS bf16x8*)(lds + (boff) + kr_st) = skr[i]; } while (0)
; #define PVO(boff) do { pv_one<0>(o0, vb0 + (boff), pa0, pa1, pa2, pa3); pv_one<1>(o1, vb0 + (boff), pa0, pa1, pa2, pa3); } while (0)
; #define SWAIT() asm volatile("s_waitcnt vmcnt(2)" ::: "memory")
; #define RESC(a) do { if (__any((a) < 1.f)) { _Pragma("unroll") for (int r = 0; r < 16; ++r) { o0[r] *= (a); o1[r] *= (a); } } } while (0)
; __device__ __forceinline__ float psm_max(const f32x16& p0, const f32x16& p1) {
;     float pmax = p0[0];
; #pragma unroll
;     for (int r = 1; r < 16; ++r) pmax = fmaxf(pmax, p0[r]);
; #pragma unroll
;     for (int r = 0; r < 16; ++r) pmax = fmaxf(pmax, p1[r]);
;     { auto rr = __builtin_amdgcn_permlane32_swap(__float_as_uint(pmax), __float_as_uint(pmax), false, false);
;       pmax = fmaxf(__uint_as_float(rr[0]), __uint_as_float(rr[1])); }
;     return pmax;
; }
; template <int DQK, bool FIXM> ...
;     ...
;     for (int j = 1; j + 1 < NT; j += 2) {
;         if (!NOBAR_PROBE) __syncthreads();
;         SBAR(); qkt<DQK>(pB0, pB1, lds + bK, qr, r32, hi, negm);
;         finishSM(pA0, pA1, alA, l_reg, pa0, pa1, pa2, pa3); SBAR();
;         SLOAD(1, j + 2); SBAR();
;         if constexpr (FIXM) pv_psm<true>(o0, o1, vb0 + bV, pa0, pa1, pa2, pa3, pB0, pB1, m_reg, negm, alB); else { PVO(bV); partialSM<false>(pB0, pB1, m_reg, negm, alB); }
;         SWAIT(); SWRITEO(bW, 0);
;         if (!FIXM) RESC(alB); ROT();
;         if (!NOBAR_PROBE) __syncthreads();
;         SBAR(); qkt<DQK>(pA0, pA1, lds + bK, qr, r32, hi, negm);
;         finishSM(pB0, pB1, alB, l_reg, pa0, pa1, pa2, pa3); SBAR();
;         if (j + 3 < NT) SLOAD(0, j + 3); SBAR();
;         if constexpr (FIXM) pv_psm<true>(o0, o1, vb0 + bV, pa0, pa1, pa2, pa3, pA0, pA1, m_reg, negm, alA); else { PVO(bV); partialSM<false>(pA0, pA1, m_reg, negm, alA); }
;         SWAIT(); SWRITEO(bW, 1);
;         if (!FIXM) RESC(alA); ROT();
;     }
.LBB0_540_0:
	v_add_f32_e32 v4, v228, v229
	v_fmac_f32_e32 v4, v227, v223
	v_add_f32_e32 v223, v126, v127
	s_add_i32 s35, s35, 2
	v_fmac_f32_e32 v223, v4, v2
	s_cmp_ge_u32 s36, s12
	s_cbranch_scc1 .Lmla_exit_0
	v_mov_b32_e32 v227, v16
	s_waitcnt lgkmcnt(0)
	s_barrier
	ds_read_b128 v[4:7], v209 offset:0
	ds_read_b128 v[8:11], v209 offset:4096
	ds_read_b128 v[174:177], v210 offset:0
	ds_read_b128 v[246:249], v210 offset:4096
	ds_read_b128 v[250:253], v211 offset:0
	ds_read_b128 v[78:81], v211 offset:4096
	ds_read_b128 v[12:15], v212 offset:0
	v_exp_f32_e32 v98, v98
	v_exp_f32_e32 v99, v99
	v_exp_f32_e32 v100, v100
	v_exp_f32_e32 v101, v101
	v_exp_f32_e32 v102, v102
	v_exp_f32_e32 v103, v103
	v_exp_f32_e32 v104, v104
	v_exp_f32_e32 v105, v105
	s_waitcnt lgkmcnt(6)
	v_mfma_f32_32x32x16_bf16 v[130:145], v[4:7], v[166:169], v[82:97]
	ds_read_b128 v[4:7], v212 offset:4096
	v_exp_f32_e32 v106, v106
	v_exp_f32_e32 v107, v107
	v_exp_f32_e32 v108, v108
	v_cvt_pk_bf16_f32 v74, v243, v245
	s_waitcnt lgkmcnt(6)
	v_mfma_f32_32x32x16_bf16 v[114:129], v[8:11], v[166:169], v[82:97]
	ds_read_b128 v[8:11], v219 offset:8192
	v_exp_f32_e32 v109, v109
	v_exp_f32_e32 v110, v110
	v_exp_f32_e32 v111, v111
	v_cvt_pk_bf16_f32 v75, v241, v244
	s_waitcnt lgkmcnt(6)
	v_mfma_f32_32x32x16_bf16 v[130:145], v[174:177], v[162:165], v[130:145]
	ds_read_b128 v[174:177], v219 offset:10240
	v_exp_f32_e32 v112, v112
	v_exp_f32_e32 v113, v113
	v_cvt_pk_bf16_f32 v76, v239, v242
	v_cvt_pk_bf16_f32 v77, v238, v240
	v_add_f32_e32 v229, 0, v243
	v_add_f32_e32 v229, v245, v229
	s_waitcnt lgkmcnt(6)
	v_mfma_f32_32x32x16_bf16 v[114:129], v[246:249], v[162:165], v[114:129]
	ds_read_b128 v[246:249], v220 offset:8192
	v_cvt_pk_bf16_f32 v66, v236, v237
	v_cvt_pk_bf16_f32 v67, v233, v235
	v_add_f32_e32 v229, v241, v229
	v_add_f32_e32 v229, v244, v229
	v_add_f32_e32 v229, v239, v229
	v_add_f32_e32 v229, v242, v229
	s_waitcnt lgkmcnt(6)
	v_mfma_f32_32x32x16_bf16 v[130:145], v[250:253], v[158:161], v[130:145]
	ds_read_b128 v[250:253], v220 offset:10240
	v_cvt_pk_bf16_f32 v68, v231, v234
	v_cvt_pk_bf16_f32 v69, v230, v232
	v_add_f32_e32 v229, v238, v229
	v_add_f32_e32 v229, v240, v229
	v_add_f32_e32 v229, v236, v229
	v_add_f32_e32 v229, v237, v229
	s_waitcnt lgkmcnt(6)
	v_mfma_f32_32x32x16_bf16 v[114:129], v[78:81], v[158:161], v[114:129]
	v_add_f32_e32 v229, v233, v229
	v_add_f32_e32 v229, v235, v229
	v_add_f32_e32 v229, v231, v229
	v_add_f32_e32 v229, v234, v229
	v_add_f32_e32 v229, v230, v229
	v_add_f32_e32 v229, v232, v229
	s_waitcnt lgkmcnt(5)
	v_mfma_f32_32x32x16_bf16 v[130:145], v[12:15], v[154:157], v[130:145]
	ds_read_b64_tr_b16 v[230:231], v213 offset:40960
	ds_read_b64_tr_b16 v[232:233], v213 offset:41984
	ds_read_b64_tr_b16 v[234:235], v213 offset:43008
	ds_read_b64_tr_b16 v[236:237], v213 offset:44032
	v_add_f32_e32 v229, v98, v229
	v_add_f32_e32 v229, v99, v229
	v_add_f32_e32 v229, v100, v229
	s_waitcnt lgkmcnt(8)
	v_mfma_f32_32x32x16_bf16 v[114:129], v[4:7], v[154:157], v[114:129]
	ds_read_b64_tr_b16 v[238:239], v213 offset:45056
	ds_read_b64_tr_b16 v[240:241], v213 offset:46080
	ds_read_b64_tr_b16 v[242:243], v213 offset:47104
	ds_read_b64_tr_b16 v[244:245], v213 offset:48128
	v_add_f32_e32 v229, v101, v229
	v_add_f32_e32 v229, v102, v229
	v_add_f32_e32 v229, v103, v229
	s_waitcnt lgkmcnt(11)
	v_mfma_f32_32x32x16_bf16 v[130:145], v[8:11], v[150:153], v[130:145]
	v_add_f32_e32 v229, v104, v229
	v_add_f32_e32 v229, v105, v229
	v_add_f32_e32 v229, v106, v229
	v_add_f32_e32 v229, v107, v229
	v_add_f32_e32 v229, v108, v229
	v_add_f32_e32 v229, v109, v229
	s_waitcnt lgkmcnt(10)
	v_mfma_f32_32x32x16_bf16 v[114:129], v[174:177], v[150:153], v[114:129]
	v_add_f32_e32 v229, v110, v229
	v_add_f32_e32 v229, v111, v229
	v_add_f32_e32 v229, v112, v229
	v_add_f32_e32 v228, v113, v229
	v_mov_b32_e32 v229, v228
	s_add_i32 s36, s35, -1
	s_cmp_lt_u32 s36, s30
	s_cselect_b32 s0, 0, s30
	s_cselect_b32 s1, s29, s34
	s_lshl_b32 s0, s0, 6
	s_sub_i32 s37, s1, s0
	s_lshl_b32 s1, s36, 6
	s_add_i32 s37, s37, s1
	s_lshl_b32 s0, s37, 6
	s_add_u32 s48, s44, s0
	s_addc_u32 s49, s45, 0
	s_lshl_b32 s0, s37, 11
	s_add_u32 s46, s42, s0
	s_addc_u32 s47, s43, 0
	global_load_dwordx4 v[174:177], v226, s[48:49]
	s_waitcnt lgkmcnt(9)
	v_mfma_f32_32x32x16_bf16 v[130:145], v[246:249], v[146:149], v[130:145]
	v_cvt_pk_bf16_f32 v70, v98, v99
	v_cvt_pk_bf16_f32 v71, v100, v101
	v_cvt_pk_bf16_f32 v72, v102, v103
	v_cvt_pk_bf16_f32 v73, v104, v105
	v_permlane32_swap_b32_e32 v228, v229
	global_load_dwordx4 v[8:11], v225, s[46:47]
	global_load_dwordx4 v[4:7], v225, s[46:47] offset:128
	s_waitcnt lgkmcnt(8)
	v_mfma_f32_32x32x16_bf16 v[114:129], v[250:253], v[146:149], v[114:129]
	v_cvt_pk_bf16_f32 v12, v106, v107
	v_cvt_pk_bf16_f32 v13, v108, v109
	v_cvt_pk_bf16_f32 v14, v110, v111
	v_cvt_pk_bf16_f32 v15, v112, v113
	ds_read_b64_tr_b16 v[78:79], v213 offset:41472
	ds_read_b64_tr_b16 v[80:81], v213 offset:42496
	ds_read_b64_tr_b16 v[98:99], v213 offset:43520
	ds_read_b64_tr_b16 v[100:101], v213 offset:44544
	ds_read_b64_tr_b16 v[102:103], v213 offset:45568
	ds_read_b64_tr_b16 v[104:105], v213 offset:46592
	ds_read_b64_tr_b16 v[110:111], v213 offset:47616
	ds_read_b64_tr_b16 v[112:113], v213 offset:48640
	v_max3_f32 v2, v130, v131, v132
	v_max3_f32 v2, v2, v133, v134
	v_max3_f32 v2, v2, v135, v136
	v_max3_f32 v2, v2, v137, v138
	v_max3_f32 v2, v2, v139, v140
	v_max3_f32 v2, v2, v141, v142
	v_max3_f32 v2, v2, v143, v144
	v_max3_f32 v2, v2, v145, v114
	v_max3_f32 v2, v2, v115, v116
	s_waitcnt lgkmcnt(8)
	v_mfma_f32_32x32x16_bf16 v[50:65], v[230:233], v[74:77], v[50:65]
	v_max3_f32 v2, v2, v117, v118
	v_max3_f32 v2, v2, v119, v120
	v_max3_f32 v2, v2, v121, v122
	v_mfma_f32_32x32x16_bf16 v[50:65], v[234:237], v[66:69], v[50:65]
	v_max3_f32 v2, v2, v123, v124
	v_max3_f32 v2, v2, v125, v126
	v_max3_f32 v2, v2, v127, v128
	v_mfma_f32_32x32x16_bf16 v[50:65], v[238:241], v[70:73], v[50:65]
	v_max_f32_e32 v2, v2, v129
	v_mfma_f32_32x32x16_bf16 v[50:65], v[242:245], v[12:15], v[50:65]
	v_cmp_ge_f32_e32 vcc, s28, v2
	s_cmp_eq_u64 vcc, exec
	s_cbranch_scc0 .LBB0_542_1
	v_mov_b32_e32 v2, 1.0

; __device__ __forceinline__ float psm_max(const f32x16& p0, const f32x16& p1) {
;     float pmax = p0[0];
; #pragma unroll
;     for (int r = 1; r < 16; ++r) pmax = fmaxf(pmax, p0[r]);
; #pragma unroll
;     for (int r = 0; r < 16; ++r) pmax = fmaxf(pmax, p1[r]);
;     { auto rr = __builtin_amdgcn_permlane32_swap(__float_as_uint(pmax), __float_as_uint(pmax), false, false);
;       pmax = fmaxf(__uint_as_float(rr[0]), __uint_as_float(rr[1])); }
;     return pmax;
; }
.Lmla_b_ld_done_1:
	s_waitcnt lgkmcnt(8)
	v_mfma_f32_32x32x16_bf16 v[98:113], v[70:73], v[146:149], v[98:113]
	v_cvt_pk_bf16_f32 v118, v122, v123
	v_cvt_pk_bf16_f32 v119, v124, v125
	v_cvt_pk_bf16_f32 v120, v126, v127
	v_cvt_pk_bf16_f32 v121, v128, v129
	v_add_f32_e32 v126, v129, v252
	v_mov_b32_e32 v127, v126
	ds_read_b64_tr_b16 v[66:67], v213 offset:512
	ds_read_b64_tr_b16 v[68:69], v213 offset:1536
	ds_read_b64_tr_b16 v[70:71], v213 offset:2560
	ds_read_b64_tr_b16 v[72:73], v213 offset:3584
	ds_read_b64_tr_b16 v[74:75], v213 offset:4608
	ds_read_b64_tr_b16 v[76:77], v213 offset:5632
	ds_read_b64_tr_b16 v[78:79], v213 offset:6656
	ds_read_b64_tr_b16 v[80:81], v213 offset:7680
	v_permlane32_swap_b32_e32 v126, v127
	v_max3_f32 v250, v130, v131, v132
	v_max3_f32 v250, v250, v133, v134
	v_max3_f32 v250, v250, v135, v136
	v_max3_f32 v250, v250, v137, v138
	v_max3_f32 v250, v250, v139, v140
	v_max3_f32 v250, v250, v141, v142
	v_max3_f32 v250, v250, v143, v144
	v_max3_f32 v250, v250, v145, v98
	v_max3_f32 v250, v250, v99, v100
	s_waitcnt lgkmcnt(8)
	v_mfma_f32_32x32x16_bf16 v[50:65], v[234:237], v[12:15], v[50:65]
	v_max3_f32 v250, v250, v101, v102
	v_max3_f32 v250, v250, v103, v104
	v_max3_f32 v250, v250, v105, v106
	v_mfma_f32_32x32x16_bf16 v[50:65], v[238:241], v[230:233], v[50:65]
	v_max3_f32 v250, v250, v107, v108
	v_max3_f32 v250, v250, v109, v110
	v_max3_f32 v250, v250, v111, v112
	v_mfma_f32_32x32x16_bf16 v[50:65], v[242:245], v[114:117], v[50:65]
	v_max_f32_e32 v250, v250, v113
	v_mfma_f32_32x32x16_bf16 v[50:65], v[246:249], v[118:121], v[50:65]
	v_cmp_ge_f32_e32 vcc, s28, v250
	s_cmp_eq_u64 vcc, exec
	v_mov_b32_e32 v16, 1.0
	s_cbranch_scc0 .LBB0_543_1

; #define SBAR() __builtin_amdgcn_sched_barrier(0)
; #define SLOAD(i, j) do { const int _row = KROW(j); skn[i] = *(const bf16x8*)(Knp + (size_t)(_row + sr) * ldk + c8 * 8); sv[i] = *(const bf16x8*)(Vp + (size_t)(_row + sr) * ldv + c8 * 8); \
;         if (krw) skr[i] = *(const bf16x8*)(Krp + (size_t)(_row + sr2) * 32 + c4 * 8); } while (0)
; #define SWRITEO(boff, i) do { *(LAS bf16x8*)(lds + (boff) + kn_st) = skn[i]; *(LAS bf16x8*)(lds + (boff) + v_stw) = sv[i]; if (krw) *(LAS bf16x8*)(lds + (boff) + kr_st) = skr[i]; } while (0)
; #define PVO(boff) do { pv_one<0>(o0, vb0 + (boff), pa0, pa1, pa2, pa3); pv_one<1>(o1, vb0 + (boff), pa0, pa1, pa2, pa3); } while (0)
; #define SWAIT() asm volatile("s_waitcnt vmcnt(2)" ::: "memory")
; #define RESC(a) do { if (__any((a) < 1.f)) { _Pragma("unroll") for (int r = 0; r < 16; ++r) { o0[r] *= (a); o1[r] *= (a); } } } while (0)
; __device__ __forceinline__ float psm_max(const f32x16& p0, const f32x16& p1) {
;     float pmax = p0[0];
; #pragma unroll
;     for (int r = 1; r < 16; ++r) pmax = fmaxf(pmax, p0[r]);
; #pragma unroll
;     for (int r = 0; r < 16; ++r) pmax = fmaxf(pmax, p1[r]);
;     { auto rr = __builtin_amdgcn_permlane32_swap(__float_as_uint(pmax), __float_as_uint(pmax), false, false);
;       pmax = fmaxf(__uint_as_float(rr[0]), __uint_as_float(rr[1])); }
;     return pmax;
; }
; template <int DQK, bool FIXM> ...
;     ...
;     for (int j = 1; j + 1 < NT; j += 2) {
;         if (!NOBAR_PROBE) __syncthreads();
;         SBAR(); qkt<DQK>(pB0, pB1, lds + bK, qr, r32, hi, negm);
;         finishSM(pA0, pA1, alA, l_reg, pa0, pa1, pa2, pa3); SBAR();
;         SLOAD(1, j + 2); SBAR();
;         if constexpr (FIXM) pv_psm<true>(o0, o1, vb0 + bV, pa0, pa1, pa2, pa3, pB0, pB1, m_reg, negm, alB); else { PVO(bV); partialSM<false>(pB0, pB1, m_reg, negm, alB); }
;         SWAIT(); SWRITEO(bW, 0);
;         if (!FIXM) RESC(alB); ROT();
;         if (!NOBAR_PROBE) __syncthreads();
;         SBAR(); qkt<DQK>(pA0, pA1, lds + bK, qr, r32, hi, negm);
;         finishSM(pB0, pB1, alB, l_reg, pa0, pa1, pa2, pa3); SBAR();
;         if (j + 3 < NT) SLOAD(0, j + 3); SBAR();
;         if constexpr (FIXM) pv_psm<true>(o0, o1, vb0 + bV, pa0, pa1, pa2, pa3, pA0, pA1, m_reg, negm, alA); else { PVO(bV); partialSM<false>(pA0, pA1, m_reg, negm, alA); }
;         SWAIT(); SWRITEO(bW, 1);
;         if (!FIXM) RESC(alA); ROT();
;     }
.LBB0_540_1:
	v_add_f32_e32 v4, v228, v229
	v_fmac_f32_e32 v4, v227, v223
	v_add_f32_e32 v223, v126, v127
	s_add_i32 s35, s35, 2
	v_fmac_f32_e32 v223, v4, v2
	s_cmp_ge_u32 s36, s12
	s_cbranch_scc1 .Lmla_exit_1
	v_mov_b32_e32 v227, v16
	s_waitcnt lgkmcnt(0)
	s_barrier
	ds_read_b128 v[4:7], v209 offset:40960
	ds_read_b128 v[8:11], v209 offset:45056
	ds_read_b128 v[174:177], v210 offset:40960
	ds_read_b128 v[246:249], v210 offset:45056
	ds_read_b128 v[250:253], v211 offset:40960
	ds_read_b128 v[78:81], v211 offset:45056
	ds_read_b128 v[12:15], v212 offset:40960
	v_exp_f32_e32 v98, v98
	v_exp_f32_e32 v99, v99
	v_exp_f32_e32 v100, v100
	v_exp_f32_e32 v101, v101
	v_exp_f32_e32 v102, v102
	v_exp_f32_e32 v103, v103
	v_exp_f32_e32 v104, v104
	v_exp_f32_e32 v105, v105
	s_waitcnt lgkmcnt(6)
	v_mfma_f32_32x32x16_bf16 v[130:145], v[4:7], v[166:169], v[82:97]
	ds_read_b128 v[4:7], v212 offset:45056
	v_exp_f32_e32 v106, v106
	v_exp_f32_e32 v107, v107
	v_exp_f32_e32 v108, v108
	v_cvt_pk_bf16_f32 v74, v243, v245
	s_waitcnt lgkmcnt(6)
	v_mfma_f32_32x32x16_bf16 v[114:129], v[8:11], v[166:169], v[82:97]
	ds_read_b128 v[8:11], v219 offset:49152
	v_exp_f32_e32 v109, v109
	v_exp_f32_e32 v110, v110
	v_exp_f32_e32 v111, v111
	v_cvt_pk_bf16_f32 v75, v241, v244
	s_waitcnt lgkmcnt(6)
	v_mfma_f32_32x32x16_bf16 v[130:145], v[174:177], v[162:165], v[130:145]
	ds_read_b128 v[174:177], v219 offset:51200
	v_exp_f32_e32 v112, v112
	v_exp_f32_e32 v113, v113
	v_cvt_pk_bf16_f32 v76, v239, v242
	v_cvt_pk_bf16_f32 v77, v238, v240
	v_add_f32_e32 v229, 0, v243
	v_add_f32_e32 v229, v245, v229
	s_waitcnt lgkmcnt(6)
	v_mfma_f32_32x32x16_bf16 v[114:129], v[246:249], v[162:165], v[114:129]
	ds_read_b128 v[246:249], v220 offset:49152
	v_cvt_pk_bf16_f32 v66, v236, v237
	v_cvt_pk_bf16_f32 v67, v233, v235
	v_add_f32_e32 v229, v241, v229
	v_add_f32_e32 v229, v244, v229
	v_add_f32_e32 v229, v239, v229
	v_add_f32_e32 v229, v242, v229
	s_waitcnt lgkmcnt(6)
	v_mfma_f32_32x32x16_bf16 v[130:145], v[250:253], v[158:161], v[130:145]
	ds_read_b128 v[250:253], v220 offset:51200
	v_cvt_pk_bf16_f32 v68, v231, v234
	v_cvt_pk_bf16_f32 v69, v230, v232
	v_add_f32_e32 v229, v238, v229
	v_add_f32_e32 v229, v240, v229
	v_add_f32_e32 v229, v236, v229
	v_add_f32_e32 v229, v237, v229
	s_waitcnt lgkmcnt(6)
	v_mfma_f32_32x32x16_bf16 v[114:129], v[78:81], v[158:161], v[114:129]
	v_add_f32_e32 v229, v233, v229
	v_add_f32_e32 v229, v235, v229
	v_add_f32_e32 v229, v231, v229
	v_add_f32_e32 v229, v234, v229
	v_add_f32_e32 v229, v230, v229
	v_add_f32_e32 v229, v232, v229
	s_waitcnt lgkmcnt(5)
	v_mfma_f32_32x32x16_bf16 v[130:145], v[12:15], v[154:157], v[130:145]
	ds_read_b64_tr_b16 v[230:231], v213 offset:20480
	ds_read_b64_tr_b16 v[232:233], v213 offset:21504
	ds_read_b64_tr_b16 v[234:235], v213 offset:22528
	ds_read_b64_tr_b16 v[236:237], v213 offset:23552
	v_add_f32_e32 v229, v98, v229
	v_add_f32_e32 v229, v99, v229
	v_add_f32_e32 v229, v100, v229
	s_waitcnt lgkmcnt(8)
	v_mfma_f32_32x32x16_bf16 v[114:129], v[4:7], v[154:157], v[114:129]
	ds_read_b64_tr_b16 v[238:239], v213 offset:24576
	ds_read_b64_tr_b16 v[240:241], v213 offset:25600
	ds_read_b64_tr_b16 v[242:243], v213 offset:26624
	ds_read_b64_tr_b16 v[244:245], v213 offset:27648
	v_add_f32_e32 v229, v101, v229
	v_add_f32_e32 v229, v102, v229
	v_add_f32_e32 v229, v103, v229
	s_waitcnt lgkmcnt(11)
	v_mfma_f32_32x32x16_bf16 v[130:145], v[8:11], v[150:153], v[130:145]
	v_add_f32_e32 v229, v104, v229
	v_add_f32_e32 v229, v105, v229
	v_add_f32_e32 v229, v106, v229
	v_add_f32_e32 v229, v107, v229
	v_add_f32_e32 v229, v108, v229
	v_add_f32_e32 v229, v109, v229
	s_waitcnt lgkmcnt(10)
	v_mfma_f32_32x32x16_bf16 v[114:129], v[174:177], v[150:153], v[114:129]
	v_add_f32_e32 v229, v110, v229
	v_add_f32_e32 v229, v111, v229
	v_add_f32_e32 v229, v112, v229
	v_add_f32_e32 v228, v113, v229
	v_mov_b32_e32 v229, v228
	s_add_i32 s36, s35, -1
	s_cmp_lt_u32 s36, s30
	s_cselect_b32 s0, 0, s30
	s_cselect_b32 s1, s29, s34
	s_lshl_b32 s0, s0, 6
	s_sub_i32 s37, s1, s0
	s_lshl_b32 s1, s36, 6
	s_add_i32 s37, s37, s1
	s_lshl_b32 s0, s37, 6
	s_add_u32 s48, s44, s0
	s_addc_u32 s49, s45, 0
	s_lshl_b32 s0, s37, 11
	s_add_u32 s46, s42, s0
	s_addc_u32 s47, s43, 0
	global_load_dwordx4 v[174:177], v226, s[48:49]
	s_waitcnt lgkmcnt(9)
	v_mfma_f32_32x32x16_bf16 v[130:145], v[246:249], v[146:149], v[130:145]
	v_cvt_pk_bf16_f32 v70, v98, v99
	v_cvt_pk_bf16_f32 v71, v100, v101
	v_cvt_pk_bf16_f32 v72, v102, v103
	v_cvt_pk_bf16_f32 v73, v104, v105
	v_permlane32_swap_b32_e32 v228, v229
	global_load_dwordx4 v[8:11], v225, s[46:47]
	global_load_dwordx4 v[4:7], v225, s[46:47] offset:128
	s_waitcnt lgkmcnt(8)
	v_mfma_f32_32x32x16_bf16 v[114:129], v[250:253], v[146:149], v[114:129]
	v_cvt_pk_bf16_f32 v12, v106, v107
	v_cvt_pk_bf16_f32 v13, v108, v109
	v_cvt_pk_bf16_f32 v14, v110, v111
	v_cvt_pk_bf16_f32 v15, v112, v113
	ds_read_b64_tr_b16 v[78:79], v213 offset:20992
	ds_read_b64_tr_b16 v[80:81], v213 offset:22016
	ds_read_b64_tr_b16 v[98:99], v213 offset:23040
	ds_read_b64_tr_b16 v[100:101], v213 offset:24064
	ds_read_b64_tr_b16 v[102:103], v213 offset:25088
	ds_read_b64_tr_b16 v[104:105], v213 offset:26112
	ds_read_b64_tr_b16 v[110:111], v213 offset:27136
	ds_read_b64_tr_b16 v[112:113], v213 offset:28160
	v_max3_f32 v2, v130, v131, v132
	v_max3_f32 v2, v2, v133, v134
	v_max3_f32 v2, v2, v135, v136
	v_max3_f32 v2, v2, v137, v138
	v_max3_f32 v2, v2, v139, v140
	v_max3_f32 v2, v2, v141, v142
	v_max3_f32 v2, v2, v143, v144
	v_max3_f32 v2, v2, v145, v114
	v_max3_f32 v2, v2, v115, v116
	s_waitcnt lgkmcnt(8)
	v_mfma_f32_32x32x16_bf16 v[50:65], v[230:233], v[74:77], v[50:65]
	v_max3_f32 v2, v2, v117, v118
	v_max3_f32 v2, v2, v119, v120
	v_max3_f32 v2, v2, v121, v122
	v_mfma_f32_32x32x16_bf16 v[50:65], v[234:237], v[66:69], v[50:65]
	v_max3_f32 v2, v2, v123, v124
	v_max3_f32 v2, v2, v125, v126
	v_max3_f32 v2, v2, v127, v128
	v_mfma_f32_32x32x16_bf16 v[50:65], v[238:241], v[70:73], v[50:65]
	v_max_f32_e32 v2, v2, v129
	v_mfma_f32_32x32x16_bf16 v[50:65], v[242:245], v[12:15], v[50:65]
	v_cmp_ge_f32_e32 vcc, s28, v2
	s_cmp_eq_u64 vcc, exec
	s_cbranch_scc0 .LBB0_542_2
	v_mov_b32_e32 v2, 1.0

; __device__ __forceinline__ float psm_max(const f32x16& p0, const f32x16& p1) {
;     float pmax = p0[0];
; #pragma unroll
;     for (int r = 1; r < 16; ++r) pmax = fmaxf(pmax, p0[r]);
; #pragma unroll
;     for (int r = 0; r < 16; ++r) pmax = fmaxf(pmax, p1[r]);
;     { auto rr = __builtin_amdgcn_permlane32_swap(__float_as_uint(pmax), __float_as_uint(pmax), false, false);
;       pmax = fmaxf(__uint_as_float(rr[0]), __uint_as_float(rr[1])); }
;     return pmax;
; }
.Lmla_b_ld_done_2:
	s_waitcnt lgkmcnt(8)
	v_mfma_f32_32x32x16_bf16 v[98:113], v[70:73], v[146:149], v[98:113]
	v_cvt_pk_bf16_f32 v118, v122, v123
	v_cvt_pk_bf16_f32 v119, v124, v125
	v_cvt_pk_bf16_f32 v120, v126, v127
	v_cvt_pk_bf16_f32 v121, v128, v129
	v_add_f32_e32 v126, v129, v252
	v_mov_b32_e32 v127, v126
	ds_read_b64_tr_b16 v[66:67], v213 offset:41472
	ds_read_b64_tr_b16 v[68:69], v213 offset:42496
	ds_read_b64_tr_b16 v[70:71], v213 offset:43520
	ds_read_b64_tr_b16 v[72:73], v213 offset:44544
	ds_read_b64_tr_b16 v[74:75], v213 offset:45568
	ds_read_b64_tr_b16 v[76:77], v213 offset:46592
	ds_read_b64_tr_b16 v[78:79], v213 offset:47616
	ds_read_b64_tr_b16 v[80:81], v213 offset:48640
	v_permlane32_swap_b32_e32 v126, v127
	v_max3_f32 v250, v130, v131, v132
	v_max3_f32 v250, v250, v133, v134
	v_max3_f32 v250, v250, v135, v136
	v_max3_f32 v250, v250, v137, v138
	v_max3_f32 v250, v250, v139, v140
	v_max3_f32 v250, v250, v141, v142
	v_max3_f32 v250, v250, v143, v144
	v_max3_f32 v250, v250, v145, v98
	v_max3_f32 v250, v250, v99, v100
	s_waitcnt lgkmcnt(8)
	v_mfma_f32_32x32x16_bf16 v[50:65], v[234:237], v[12:15], v[50:65]
	v_max3_f32 v250, v250, v101, v102
	v_max3_f32 v250, v250, v103, v104
	v_max3_f32 v250, v250, v105, v106
	v_mfma_f32_32x32x16_bf16 v[50:65], v[238:241], v[230:233], v[50:65]
	v_max3_f32 v250, v250, v107, v108
	v_max3_f32 v250, v250, v109, v110
	v_max3_f32 v250, v250, v111, v112
	v_mfma_f32_32x32x16_bf16 v[50:65], v[242:245], v[114:117], v[50:65]
	v_max_f32_e32 v250, v250, v113
	v_mfma_f32_32x32x16_bf16 v[50:65], v[246:249], v[118:121], v[50:65]
	v_cmp_ge_f32_e32 vcc, s28, v250
	s_cmp_eq_u64 vcc, exec
	v_mov_b32_e32 v16, 1.0
	s_cbranch_scc0 .LBB0_543_2

; template <bool FIRST> __device__ __forceinline__ void psm_apply(f32x16& p0, f32x16& p1, float pmax, float& m_reg, f32x16& negm, float& alpha) {
;     alpha = 1.f;
;     if (FIRST || !__builtin_expect(__all(pmax <= THR2), 1)) {
;         const float delta = FIRST ? pmax : fmaxf(pmax, 0.f);
;         if (!FIRST) alpha = __builtin_amdgcn_exp2f(-delta);
;         m_reg += delta;
; #pragma unroll
;         for (int r = 0; r < 16; ++r) { p0[r] -= delta; p1[r] -= delta; negm[r] = -m_reg; }
;     }
.LBB0_542_0:
	v_mov_b32_e32 v16, v2
	s_nop 1
	v_permlane32_swap_b32_e32 v2, v16
	v_max_f32_e32 v2, v2, v16
	v_max_f32_e32 v2, v2, v2
	v_max_f32_e32 v16, 0, v2
	v_exp_f32_e64 v2, -v16
	v_add_f32_e32 v224, v224, v16
	v_xor_b32_e32 v82, 0x80000000, v224
	v_pk_add_f32 v[130:131], v[130:131], v[16:17] op_sel_hi:[1,0] neg_lo:[0,1] neg_hi:[0,1]
	v_pk_add_f32 v[132:133], v[132:133], v[16:17] op_sel_hi:[1,0] neg_lo:[0,1] neg_hi:[0,1]
	v_pk_add_f32 v[134:135], v[134:135], v[16:17] op_sel_hi:[1,0] neg_lo:[0,1] neg_hi:[0,1]
	v_pk_add_f32 v[136:137], v[136:137], v[16:17] op_sel_hi:[1,0] neg_lo:[0,1] neg_hi:[0,1]
	v_pk_add_f32 v[138:139], v[138:139], v[16:17] op_sel_hi:[1,0] neg_lo:[0,1] neg_hi:[0,1]
	v_pk_add_f32 v[140:141], v[140:141], v[16:17] op_sel_hi:[1,0] neg_lo:[0,1] neg_hi:[0,1]
	v_pk_add_f32 v[142:143], v[142:143], v[16:17] op_sel_hi:[1,0] neg_lo:[0,1] neg_hi:[0,1]
	v_pk_add_f32 v[144:145], v[144:145], v[16:17] op_sel_hi:[1,0] neg_lo:[0,1] neg_hi:[0,1]
	v_sub_f32_e32 v129, v129, v16
	v_sub_f32_e32 v128, v128, v16
	v_sub_f32_e32 v127, v127, v16
	v_sub_f32_e32 v126, v126, v16
	v_sub_f32_e32 v125, v125, v16
	v_sub_f32_e32 v124, v124, v16
	v_sub_f32_e32 v123, v123, v16
	v_sub_f32_e32 v122, v122, v16
	v_sub_f32_e32 v121, v121, v16
	v_sub_f32_e32 v120, v120, v16
	v_sub_f32_e32 v119, v119, v16
	v_sub_f32_e32 v118, v118, v16
	v_sub_f32_e32 v117, v117, v16
	v_sub_f32_e32 v116, v116, v16
	v_sub_f32_e32 v115, v115, v16
	v_sub_f32_e32 v114, v114, v16
	v_mov_b32_e32 v83, v82
	v_mov_b32_e32 v84, v82
	v_mov_b32_e32 v85, v82
	v_mov_b32_e32 v86, v82
	v_mov_b32_e32 v87, v82
	v_mov_b32_e32 v88, v82
	v_mov_b32_e32 v89, v82
	v_mov_b32_e32 v90, v82
	v_mov_b32_e32 v91, v82
	v_mov_b32_e32 v92, v82
	v_mov_b32_e32 v93, v82
	v_mov_b32_e32 v94, v82
	v_mov_b32_e32 v95, v82
	v_mov_b32_e32 v96, v82
	v_mov_b32_e32 v97, v82
	s_branch .LBB0_527_0
.LBB0_543_0:
	v_mov_b32_e32 v251, v250
	s_nop 1
	v_permlane32_swap_b32_e32 v250, v251
	v_max_f32_e32 v250, v250, v251
	v_max_f32_e32 v250, v250, v250
	v_max_f32_e32 v250, 0, v250
	v_exp_f32_e64 v16, -v250
	v_add_f32_e32 v224, v224, v250
	v_xor_b32_e32 v82, 0x80000000, v224
	v_pk_add_f32 v[130:131], v[130:131], v[250:251] op_sel_hi:[1,0] neg_lo:[0,1] neg_hi:[0,1]
	v_pk_add_f32 v[132:133], v[132:133], v[250:251] op_sel_hi:[1,0] neg_lo:[0,1] neg_hi:[0,1]
	v_pk_add_f32 v[134:135], v[134:135], v[250:251] op_sel_hi:[1,0] neg_lo:[0,1] neg_hi:[0,1]
	v_pk_add_f32 v[136:137], v[136:137], v[250:251] op_sel_hi:[1,0] neg_lo:[0,1] neg_hi:[0,1]
	v_pk_add_f32 v[138:139], v[138:139], v[250:251] op_sel_hi:[1,0] neg_lo:[0,1] neg_hi:[0,1]
	v_pk_add_f32 v[140:141], v[140:141], v[250:251] op_sel_hi:[1,0] neg_lo:[0,1] neg_hi:[0,1]
	v_pk_add_f32 v[142:143], v[142:143], v[250:251] op_sel_hi:[1,0] neg_lo:[0,1] neg_hi:[0,1]
	v_pk_add_f32 v[144:145], v[144:145], v[250:251] op_sel_hi:[1,0] neg_lo:[0,1] neg_hi:[0,1]
	v_sub_f32_e32 v113, v113, v250
	v_sub_f32_e32 v112, v112, v250
	v_sub_f32_e32 v111, v111, v250
	v_sub_f32_e32 v110, v110, v250
	v_sub_f32_e32 v109, v109, v250
	v_sub_f32_e32 v108, v108, v250
	v_sub_f32_e32 v107, v107, v250
	v_sub_f32_e32 v106, v106, v250
	v_sub_f32_e32 v105, v105, v250
	v_sub_f32_e32 v104, v104, v250
	v_sub_f32_e32 v103, v103, v250
	v_sub_f32_e32 v102, v102, v250
	v_sub_f32_e32 v101, v101, v250
	v_sub_f32_e32 v100, v100, v250
	v_sub_f32_e32 v99, v99, v250
	v_sub_f32_e32 v98, v98, v250
	v_mov_b32_e32 v83, v82
	v_mov_b32_e32 v84, v82
	v_mov_b32_e32 v85, v82
	v_mov_b32_e32 v86, v82
	v_mov_b32_e32 v87, v82
	v_mov_b32_e32 v88, v82
	v_mov_b32_e32 v89, v82
	v_mov_b32_e32 v90, v82
	v_mov_b32_e32 v91, v82
	v_mov_b32_e32 v92, v82
	v_mov_b32_e32 v93, v82
	v_mov_b32_e32 v94, v82
	v_mov_b32_e32 v95, v82
	v_mov_b32_e32 v96, v82
	v_mov_b32_e32 v97, v82
	s_branch .LBB0_536_0
